# stick-breaking scan: cross-half exchange via v_permlane32_swap (VALU) instead of ds_bpermute on the serial carry chain, 16 sites
# speedup vs baseline: 1.0002x; 1.0002x over previous
; #define LAS __attribute__((address_space(3)))
; template <int BR>
; DI void unit(LAS unsigned char* lds, const bf16* __restrict__ Q, const bf16* __restrict__ Kx, const bf16* __restrict__ VT, const bf16* __restrict__ RG, const bf16* __restrict__ RG1, bf16* __restrict__ O, int b, int h, int qb) {
;     ...
;                 const int kt = 1 - kk;
;                 f32x16 sT;
; #pragma unroll
;                 for (int i = 0; i < 16; ++i) sT[i] = 0.f;
; #pragma unroll
;                 for (int ks = 0; ks < 8; ++ks) { const bf16x8 a = *(const LAS bf16x8*)(kb_ + kt * 32 * KS_ + 32 * ks); sT = __builtin_amdgcn_mfma_f32_32x32x16_bf16(a, qf[ks], sT, 0, 0, 0); }
;                 float w[16];
;                 if (BR == 1) {
; #pragma unroll
;                     for (int gg = 0; gg < 4; ++gg) {
;                         const int g = 3 - gg;
;                         float lf[4], ls[4]; bool vd_[4];
; #pragma unroll
;                         for (int e = 0; e < 4; ++e) {
;                             const float z2 = __builtin_amdgcn_fmed3f(sT[4 * g + e] * C2, -126.f, 126.f);
;                             const float ex = __builtin_amdgcn_exp2f(z2); const float sp = __builtin_amdgcn_logf(1.0f + ex);
;                             vd_[e] = (32 * kt + 8 * g + e) < tq; lf[e] = vd_[e] ? -sp : 0.f; ls[e] = z2 - sp;
;                         }
;                         const float s2 = lf[3], s1 = s2 + lf[2], s0x = s1 + lf[1], T = s0x + lf[0];
;                         const float Tp = __shfl_xor(T, 32);
;                         const float off = carry + (hf == 0 ? Tp : 0.f);
;                         w[4 * g + 3] = vd_[3] ? __builtin_amdgcn_exp2f(ls[3] + off) : 0.f;
;                         w[4 * g + 2] = vd_[2] ? __builtin_amdgcn_exp2f(ls[2] + (off + s2)) : 0.f;
;                         w[4 * g + 1] = vd_[1] ? __builtin_amdgcn_exp2f(ls[1] + (off + s1)) : 0.f;
;                         w[4 * g + 0] = vd_[0] ? __builtin_amdgcn_exp2f(ls[0] + (off + s0x)) : 0.f;
;                         carry += T + Tp;
;                     }
.LBB0_391:
	s_cmp_gt_i32 s88, s75
	s_cselect_b64 s[10:11], -1, 0
	s_or_b64 s[10:11], s[10:11], s[8:9]
	s_and_b64 vcc, exec, s[10:11]
	s_cbranch_vccnz .LBB0_393
	v_add3_u32 v168, s91, v146, v144
	ds_read_b128 v[64:67], v168 offset:8704
	ds_read_b128 v[150:153], v168 offset:8736
	v_and_b32_e32 v82, 64, v195
	v_xor_b32_e32 v81, 32, v195
	v_add_u32_e32 v82, 64, v82
	s_waitcnt lgkmcnt(1)
	v_mfma_f32_32x32x16_bf16 v[64:79], v[64:67], v[84:87], 0
	v_cmp_lt_i32_e32 vcc, v81, v82
	v_cmp_lt_i32_e64 s[12:13], 56, v149
	v_cmp_lt_i32_e64 s[14:15], 57, v149
	v_cndmask_b32_e32 v81, v195, v81, vcc
	v_cmp_lt_i32_e64 s[16:17], 58, v149
	v_cmp_lt_i32_e64 s[18:19], 59, v149
	v_cmp_lt_i32_e64 s[10:11], 50, v149
	s_waitcnt lgkmcnt(0)
	v_mfma_f32_32x32x16_bf16 v[64:79], v[150:153], v[88:91], v[64:79]
	ds_read_b128 v[150:153], v168 offset:8768
	ds_read_b128 v[154:157], v168 offset:8800
	v_cmp_lt_i32_e64 s[20:21], 51, v149
	v_cmp_lt_i32_e64 s[8:9], 49, v149
	v_cmp_lt_i32_e32 vcc, 48, v149
	v_cmp_lt_i32_e64 s[22:23], 27, v149
	v_cmp_lt_i32_e64 s[24:25], 10, v149
	v_cmp_lt_i32_e64 s[26:27], 11, v149
	s_waitcnt lgkmcnt(1)
	v_mfma_f32_32x32x16_bf16 v[64:79], v[150:153], v[92:95], v[64:79]
	v_cmp_lt_i32_e64 s[28:29], 3, v149
	s_waitcnt lgkmcnt(0)
	v_mfma_f32_32x32x16_bf16 v[64:79], v[154:157], v[96:99], v[64:79]
	ds_read_b128 v[150:153], v168 offset:8832
	ds_read_b128 v[154:157], v168 offset:8864
	s_waitcnt lgkmcnt(1)
	v_mfma_f32_32x32x16_bf16 v[64:79], v[150:153], v[100:103], v[64:79]
	s_waitcnt lgkmcnt(0)
	v_mfma_f32_32x32x16_bf16 v[64:79], v[154:157], v[104:107], v[64:79]
	ds_read_b128 v[150:153], v168 offset:8896
	ds_read_b128 v[154:157], v168 offset:8928
	s_waitcnt lgkmcnt(1)
	v_mfma_f32_32x32x16_bf16 v[64:79], v[150:153], v[108:111], v[64:79]
	v_lshlrev_b32_e32 v150, 2, v81
	s_waitcnt lgkmcnt(0)
	v_mfma_f32_32x32x16_bf16 v[64:79], v[154:157], v[112:115], v[64:79]
	s_nop 11
	v_mul_f32_e32 v76, 0x3e0293ee, v76
	v_mul_f32_e32 v77, 0x3e0293ee, v77
	v_mul_f32_e32 v78, 0x3e0293ee, v78
	v_mul_f32_e32 v79, 0x3e0293ee, v79
	v_med3_f32 v76, v76, s79, v196
	v_med3_f32 v77, v77, s79, v196
	v_med3_f32 v78, v78, s79, v196
	v_med3_f32 v79, v79, s79, v196
	v_exp_f32_e32 v81, v76
	v_exp_f32_e32 v82, v77
	v_exp_f32_e32 v83, v78
	v_exp_f32_e32 v151, v79
	v_mul_f32_e32 v72, 0x3e0293ee, v72
	v_med3_f32 v72, v72, s79, v196
	v_exp_f32_e32 v152, v72
	v_add_f32_e32 v81, 1.0, v81
	v_add_f32_e32 v82, 1.0, v82
	v_add_f32_e32 v83, 1.0, v83
	v_add_f32_e32 v151, 1.0, v151
	v_log_f32_e32 v81, v81
	v_log_f32_e32 v82, v82
	v_log_f32_e32 v83, v83
	v_log_f32_e32 v151, v151
	v_add_f32_e32 v152, 1.0, v152
	v_log_f32_e32 v156, v152
	v_cndmask_b32_e64 v152, 0, -v81, s[12:13]
	v_sub_f32_e32 v76, v76, v81
	v_cndmask_b32_e64 v81, 0, -v82, s[14:15]
	v_sub_f32_e32 v77, v77, v82
	v_cndmask_b32_e64 v82, 0, -v83, s[16:17]
	v_sub_f32_e32 v78, v78, v83
	v_cndmask_b32_e64 v83, 0, -v151, s[18:19]
	v_add_f32_e32 v82, v83, v82
	v_add_f32_e32 v81, v81, v82
	v_add_f32_e32 v160, v152, v81
	v_mov_b32_e32 v161, v160
	s_nop 1
	v_permlane32_swap_b32_e32 v160, v161
	v_mul_f32_e32 v74, 0x3e0293ee, v74
	v_mul_f32_e32 v75, 0x3e0293ee, v75
	v_mul_f32_e32 v73, 0x3e0293ee, v73
	v_med3_f32 v74, v74, s79, v196
	v_med3_f32 v75, v75, s79, v196
	v_med3_f32 v73, v73, s79, v196
	v_exp_f32_e32 v154, v74
	v_exp_f32_e32 v155, v75
	v_exp_f32_e32 v153, v73
	v_sub_f32_e32 v79, v79, v151
	s_waitcnt lgkmcnt(0)
	v_cndmask_b32_e64 v151, 0, v161, s[4:5]
	v_add_f32_e32 v151, v80, v151
	v_add_f32_e32 v154, 1.0, v154
	v_add_f32_e32 v155, 1.0, v155
	v_add_f32_e32 v82, v151, v82
	v_add_f32_e32 v153, 1.0, v153
	v_log_f32_e32 v158, v154
	v_log_f32_e32 v155, v155
	v_add_f32_e32 v83, v151, v83
	v_add_f32_e32 v77, v77, v82
	v_log_f32_e32 v157, v153
	v_add_f32_e32 v78, v78, v83
	v_exp_f32_e32 v77, v77
	v_add_f32_e32 v79, v151, v79
	v_exp_f32_e32 v78, v78
	v_exp_f32_e32 v79, v79
	v_cndmask_b32_e64 v162, 0, -v158, s[10:11]
	v_cndmask_b32_e64 v163, 0, -v155, s[20:21]
	v_cndmask_b32_e64 v159, 0, -v157, s[8:9]
	v_cndmask_b32_e64 v153, 0, v77, s[14:15]
	v_add_f32_e32 v77, v163, v162
	v_cndmask_b32_e64 v154, 0, -v156, vcc
	v_add_f32_e32 v81, v151, v81
	v_cndmask_b32_e64 v152, 0, v78, s[16:17]
	v_add_f32_e32 v78, v159, v77
	v_add_f32_e32 v76, v76, v81
	v_cndmask_b32_e64 v151, 0, v79, s[18:19]
	v_add_f32_e32 v79, v154, v78
	v_exp_f32_e32 v76, v76
	v_mov_b32_e32 v81, v79
	s_nop 1
	v_permlane32_swap_b32_e32 v79, v81
	v_sub_f32_e32 v75, v75, v155
	v_sub_f32_e32 v74, v74, v158
	v_cndmask_b32_e64 v154, 0, v76, s[12:13]
	v_add_f32_e32 v76, v160, v161
	v_add_f32_e32 v76, v80, v76
	s_waitcnt lgkmcnt(0)
	v_cndmask_b32_e64 v80, 0, v81, s[4:5]
	v_add_f32_e32 v80, v80, v76
	v_add_f32_e32 v75, v75, v80
	v_exp_f32_e32 v75, v75
	v_sub_f32_e32 v72, v72, v156
	v_sub_f32_e32 v73, v73, v157
	v_mul_f32_e32 v68, 0x3e0293ee, v68
	v_cndmask_b32_e64 v155, 0, v75, s[20:21]
	v_add_f32_e32 v75, v163, v80
	v_add_f32_e32 v74, v74, v75
	v_exp_f32_e32 v156, v74
	v_add_f32_e32 v74, v77, v80
	v_add_f32_e32 v73, v73, v74
	v_med3_f32 v68, v68, s79, v196
	v_exp_f32_e32 v157, v73
	v_exp_f32_e32 v73, v68
	v_mul_f32_e32 v70, 0x3e0293ee, v70
	v_mul_f32_e32 v71, 0x3e0293ee, v71
	v_add_f32_e32 v74, v78, v80
	v_mul_f32_e32 v69, 0x3e0293ee, v69
	v_med3_f32 v70, v70, s79, v196
	v_med3_f32 v71, v71, s79, v196
	v_add_f32_e32 v72, v72, v74
	v_med3_f32 v69, v69, s79, v196
	v_exp_f32_e32 v77, v70
	v_exp_f32_e32 v78, v71
	v_exp_f32_e32 v158, v72
	v_add_f32_e32 v72, 1.0, v73
	v_exp_f32_e32 v73, v69
	v_add_f32_e32 v77, 1.0, v77
	v_add_f32_e32 v78, 1.0, v78
	v_log_f32_e32 v77, v77
	v_add_f32_e32 v73, 1.0, v73
	v_log_f32_e32 v78, v78
	v_log_f32_e32 v73, v73
	v_log_f32_e32 v72, v72
	v_cmp_lt_i32_e64 s[16:17], 42, v149
	v_cmp_lt_i32_e64 s[18:19], 43, v149
	v_add_f32_e32 v74, v79, v81
	v_cmp_lt_i32_e64 s[14:15], 41, v149
	v_cndmask_b32_e64 v80, 0, -v77, s[16:17]
	v_cndmask_b32_e64 v81, 0, -v78, s[18:19]
	v_cmp_lt_i32_e64 s[12:13], 40, v149
	v_cndmask_b32_e64 v79, 0, -v73, s[14:15]
	v_add_f32_e32 v80, v81, v80
	v_cndmask_b32_e64 v75, 0, -v72, s[12:13]
	v_add_f32_e32 v79, v79, v80
	v_add_f32_e32 v169, v75, v79
	v_mov_b32_e32 v170, v169
	s_nop 1
	v_permlane32_swap_b32_e32 v169, v170
	v_add_f32_e32 v171, v74, v76
	v_sub_f32_e32 v69, v69, v73
	v_sub_f32_e32 v70, v70, v77
	v_sub_f32_e32 v71, v71, v78
	s_waitcnt lgkmcnt(0)
; #define LAS __attribute__((address_space(3)))
; template <int BR>
; DI void unit(LAS unsigned char* lds, const bf16* __restrict__ Q, const bf16* __restrict__ Kx, const bf16* __restrict__ VT, const bf16* __restrict__ RG, const bf16* __restrict__ RG1, bf16* __restrict__ O, int b, int h, int qb) {
;     ...
;                 for (int ks = 0; ks < 8; ++ks) { const bf16x8 a = *(const LAS bf16x8*)(kb_ + kt * 32 * KS_ + 32 * ks); sT = __builtin_amdgcn_mfma_f32_32x32x16_bf16(a, qf[ks], sT, 0, 0, 0); }
;                 float w[16];
;                 if (BR == 1) {
; #pragma unroll
;                     for (int gg = 0; gg < 4; ++gg) {
;                         const int g = 3 - gg;
;                         float lf[4], ls[4]; bool vd_[4];
; #pragma unroll
;                         for (int e = 0; e < 4; ++e) {
;                             const float z2 = __builtin_amdgcn_fmed3f(sT[4 * g + e] * C2, -126.f, 126.f);
;                             const float ex = __builtin_amdgcn_exp2f(z2); const float sp = __builtin_amdgcn_logf(1.0f + ex);
;                             vd_[e] = (32 * kt + 8 * g + e) < tq; lf[e] = vd_[e] ? -sp : 0.f; ls[e] = z2 - sp;
;                         }
;                         const float s2 = lf[3], s1 = s2 + lf[2], s0x = s1 + lf[1], T = s0x + lf[0];
;                         const float Tp = __shfl_xor(T, 32);
;                         const float off = carry + (hf == 0 ? Tp : 0.f);
;                         w[4 * g + 3] = vd_[3] ? __builtin_amdgcn_exp2f(ls[3] + off) : 0.f;
;                         w[4 * g + 2] = vd_[2] ? __builtin_amdgcn_exp2f(ls[2] + (off + s2)) : 0.f;
;                         w[4 * g + 1] = vd_[1] ? __builtin_amdgcn_exp2f(ls[1] + (off + s1)) : 0.f;
;                         w[4 * g + 0] = vd_[0] ? __builtin_amdgcn_exp2f(ls[0] + (off + s0x)) : 0.f;
;                         carry += T + Tp;
;                     }
	v_cndmask_b32_e64 v73, 0, v170, s[4:5]
	v_add_f32_e32 v73, v73, v171
	v_add_f32_e32 v74, v81, v73
	v_add_f32_e32 v70, v70, v74
	v_add_f32_e32 v74, v80, v73
	v_add_f32_e32 v71, v71, v73
	v_add_f32_e32 v69, v69, v74
	v_exp_f32_e32 v71, v71
	v_exp_f32_e32 v70, v70
	v_exp_f32_e32 v69, v69
	v_sub_f32_e32 v72, v68, v72
	v_cndmask_b32_e64 v159, 0, v71, s[18:19]
	v_cndmask_b32_e64 v172, 0, v70, s[16:17]
	v_cndmask_b32_e64 v173, 0, v69, s[14:15]
	ds_read_b128 v[68:71], v168
	ds_read_b128 v[160:163], v168 offset:32
	v_add_f32_e32 v73, v79, v73
	v_mul_f32_e32 v64, 0x3e0293ee, v64
	v_add_f32_e32 v72, v72, v73
	v_med3_f32 v174, v64, s79, v196
	v_exp_f32_e32 v164, v72
	s_waitcnt lgkmcnt(1)
	v_mfma_f32_32x32x16_bf16 v[68:83], v[68:71], v[84:87], 0
	v_exp_f32_e32 v64, v174
	v_cndmask_b32_e64 v177, 0, v164, s[12:13]
	ds_read_b128 v[164:167], v168 offset:64
	v_cmp_lt_i32_e64 s[16:17], 34, v149
	v_add_f32_e32 v64, 1.0, v64
	v_log_f32_e32 v175, v64
	v_mul_f32_e32 v64, 0x3e0293ee, v65
	v_med3_f32 v176, v64, s79, v196
	v_exp_f32_e32 v64, v176
	s_waitcnt lgkmcnt(1)
	v_mfma_f32_32x32x16_bf16 v[68:83], v[160:163], v[88:91], v[68:83]
	v_cmp_lt_i32_e64 s[18:19], 35, v149
	v_cmp_lt_i32_e64 s[14:15], 33, v149
	v_add_f32_e32 v64, 1.0, v64
	v_log_f32_e32 v179, v64
	v_mul_f32_e32 v64, 0x3e0293ee, v66
	v_med3_f32 v180, v64, s79, v196
	v_mul_f32_e32 v64, 0x3e0293ee, v67
	v_med3_f32 v181, v64, s79, v196
	ds_read_b128 v[64:67], v168 offset:96
	s_waitcnt lgkmcnt(1)
	v_mfma_f32_32x32x16_bf16 v[68:83], v[164:167], v[92:95], v[68:83]
	v_exp_f32_e32 v160, v180
	v_exp_f32_e32 v161, v181
	v_cndmask_b32_e64 v162, 0, -v179, s[14:15]
	v_cmp_lt_i32_e64 s[12:13], 32, v149
	v_add_f32_e32 v160, 1.0, v160
	v_log_f32_e32 v164, v160
	v_add_f32_e32 v160, 1.0, v161
	s_waitcnt lgkmcnt(0)
	v_mfma_f32_32x32x16_bf16 v[68:83], v[64:67], v[96:99], v[68:83]
	ds_read_b128 v[64:67], v168 offset:128
	v_log_f32_e32 v165, v160
	v_cndmask_b32_e64 v160, 0, -v164, s[16:17]
	v_cndmask_b32_e64 v178, 0, -v175, s[12:13]
	v_sub_f32_e32 v164, v180, v164
	v_cndmask_b32_e64 v166, 0, -v165, s[18:19]
	v_add_f32_e32 v167, v166, v160
	v_add_f32_e32 v182, v162, v167
	ds_read_b128 v[160:163], v168 offset:160
	s_waitcnt lgkmcnt(1)
	v_mfma_f32_32x32x16_bf16 v[68:83], v[64:67], v[100:103], v[68:83]
	v_add_f32_e32 v178, v178, v182
	v_mov_b32_e32 v183, v178
	s_nop 1
	v_permlane32_swap_b32_e32 v178, v183
	v_add_f32_e32 v64, v169, v170
	v_add_f32_e32 v169, v64, v171
	ds_read_b128 v[64:67], v168 offset:192
	v_sub_f32_e32 v165, v181, v165
	s_waitcnt lgkmcnt(1)
	v_cndmask_b32_e64 v170, 0, v183, s[4:5]
	v_mfma_f32_32x32x16_bf16 v[68:83], v[160:163], v[104:107], v[68:83]
	v_add_f32_e32 v170, v170, v169
	v_add_f32_e32 v160, v165, v170
	v_exp_f32_e32 v165, v160
	v_add_f32_e32 v160, v166, v170
	v_add_f32_e32 v160, v164, v160
	v_exp_f32_e32 v164, v160
	ds_read_b128 v[160:163], v168 offset:224
	s_waitcnt lgkmcnt(1)
	v_mfma_f32_32x32x16_bf16 v[68:83], v[64:67], v[108:111], v[68:83]
	v_sub_f32_e32 v65, v176, v179
	v_add_f32_e32 v66, v167, v170
	v_add_f32_e32 v65, v65, v66
	v_exp_f32_e32 v166, v65
	v_sub_f32_e32 v64, v174, v175
	v_add_f32_e32 v67, v182, v170
	v_add_f32_e32 v64, v64, v67
	s_waitcnt lgkmcnt(0)
	v_mfma_f32_32x32x16_bf16 v[68:83], v[160:163], v[112:115], v[68:83]
	v_cmp_lt_i32_e64 s[20:21], 26, v149
	v_cndmask_b32_e64 v165, 0, v165, s[18:19]
	v_cmp_lt_i32_e64 s[18:19], 25, v149
	v_cndmask_b32_e64 v164, 0, v164, s[16:17]
	v_cmp_lt_i32_e64 s[16:17], 24, v149
	s_nop 6
	v_mul_f32_e32 v65, 0x3e0293ee, v80
	v_med3_f32 v65, v65, s79, v196
	v_exp_f32_e32 v66, v65
	v_mul_f32_e32 v82, 0x3e0293ee, v82
	v_mul_f32_e32 v83, 0x3e0293ee, v83
	v_exp_f32_e32 v80, v64
	v_add_f32_e32 v64, 1.0, v66
	v_mul_f32_e32 v66, 0x3e0293ee, v81
	v_med3_f32 v82, v82, s79, v196
	v_med3_f32 v83, v83, s79, v196
	v_med3_f32 v66, v66, s79, v196
	v_exp_f32_e32 v161, v82
	v_exp_f32_e32 v162, v83
	v_exp_f32_e32 v67, v66
	v_log_f32_e32 v64, v64
	v_add_f32_e32 v161, 1.0, v161
	v_add_f32_e32 v162, 1.0, v162
	v_add_f32_e32 v67, 1.0, v67
	v_log_f32_e32 v161, v161
	v_log_f32_e32 v162, v162
	v_log_f32_e32 v67, v67
	v_cndmask_b32_e64 v160, 0, -v64, s[16:17]
	v_cndmask_b32_e64 v167, 0, -v161, s[20:21]
	v_cndmask_b32_e64 v168, 0, -v162, s[22:23]
	v_cndmask_b32_e64 v163, 0, -v67, s[18:19]
	v_add_f32_e32 v167, v168, v167
	v_add_f32_e32 v163, v163, v167
	v_add_f32_e32 v160, v160, v163
	v_mov_b32_e32 v170, v160
	s_nop 1
	v_permlane32_swap_b32_e32 v160, v170
	v_add_f32_e32 v81, v178, v183
	v_add_f32_e32 v81, v81, v169
	v_sub_f32_e32 v66, v66, v67
	v_sub_f32_e32 v67, v82, v161
	v_sub_f32_e32 v82, v83, v162
	s_waitcnt lgkmcnt(0)
	v_cndmask_b32_e64 v83, 0, v170, s[4:5]
	v_add_f32_e32 v83, v81, v83
	v_add_f32_e32 v161, v83, v168
	v_add_f32_e32 v67, v67, v161
	v_exp_f32_e32 v67, v67
	v_add_f32_e32 v161, v83, v167
	v_add_f32_e32 v66, v66, v161
	v_exp_f32_e32 v66, v66
	v_sub_f32_e32 v64, v65, v64
	v_cndmask_b32_e64 v161, 0, v67, s[20:21]
	v_add_f32_e32 v67, v83, v163
	v_mul_f32_e32 v78, 0x3e0293ee, v78
	v_mul_f32_e32 v79, 0x3e0293ee, v79
	v_add_f32_e32 v64, v64, v67
	v_mul_f32_e32 v67, 0x3e0293ee, v77
	v_med3_f32 v78, v78, s79, v196
	v_med3_f32 v79, v79, s79, v196
	v_add_f32_e32 v82, v83, v82
	v_mul_f32_e32 v65, 0x3e0293ee, v76
	v_med3_f32 v67, v67, s79, v196
	v_exp_f32_e32 v83, v78
	v_exp_f32_e32 v163, v79
	v_med3_f32 v65, v65, s79, v196
	v_exp_f32_e32 v76, v67
	v_cndmask_b32_e64 v162, 0, v66, s[18:19]
	v_exp_f32_e32 v66, v65
	v_exp_f32_e32 v82, v82
	v_add_f32_e32 v83, 1.0, v83
	v_add_f32_e32 v163, 1.0, v163
	v_add_f32_e32 v76, 1.0, v76
	v_log_f32_e32 v83, v83
	v_log_f32_e32 v163, v163
	v_exp_f32_e32 v64, v64
	v_add_f32_e32 v66, 1.0, v66
	v_log_f32_e32 v76, v76
	v_log_f32_e32 v66, v66
	v_cndmask_b32_e64 v82, 0, v82, s[22:23]
	v_cmp_lt_i32_e64 s[20:21], 18, v149
	v_cmp_lt_i32_e64 s[22:23], 19, v149
	v_cmp_lt_i32_e64 s[18:19], 17, v149
	v_cndmask_b32_e64 v168, 0, -v83, s[20:21]
	v_cndmask_b32_e64 v169, 0, -v163, s[22:23]
	v_cndmask_b32_e64 v77, 0, v64, s[16:17]
	v_cmp_lt_i32_e64 s[16:17], 16, v149
	v_cndmask_b32_e64 v167, 0, -v76, s[18:19]
	v_add_f32_e32 v168, v169, v168
	v_cndmask_b32_e64 v64, 0, -v66, s[16:17]
	v_add_f32_e32 v167, v167, v168
	v_add_f32_e32 v64, v64, v167
	v_mov_b32_e32 v171, v64
	s_nop 1
	v_permlane32_swap_b32_e32 v64, v171
	v_add_f32_e32 v160, v160, v170
	v_add_f32_e32 v81, v81, v160
	v_sub_f32_e32 v78, v78, v83
	v_sub_f32_e32 v79, v79, v163
	s_waitcnt lgkmcnt(0)
; template <int BR>
; DI void unit(LAS unsigned char* lds, const bf16* __restrict__ Q, const bf16* __restrict__ Kx, const bf16* __restrict__ VT, const bf16* __restrict__ RG, const bf16* __restrict__ RG1, bf16* __restrict__ O, int b, int h, int qb) {
;     ...
;                     for (int gg = 0; gg < 4; ++gg) {
;                         const int g = 3 - gg;
;                         float lf[4], ls[4]; bool vd_[4];
; #pragma unroll
;                         for (int e = 0; e < 4; ++e) {
;                             const float z2 = __builtin_amdgcn_fmed3f(sT[4 * g + e] * C2, -126.f, 126.f);
;                             const float ex = __builtin_amdgcn_exp2f(z2); const float sp = __builtin_amdgcn_logf(1.0f + ex);
;                             vd_[e] = (32 * kt + 8 * g + e) < tq; lf[e] = vd_[e] ? -sp : 0.f; ls[e] = z2 - sp;
;                         }
;                         const float s2 = lf[3], s1 = s2 + lf[2], s0x = s1 + lf[1], T = s0x + lf[0];
;                         const float Tp = __shfl_xor(T, 32);
;                         const float off = carry + (hf == 0 ? Tp : 0.f);
;                         w[4 * g + 3] = vd_[3] ? __builtin_amdgcn_exp2f(ls[3] + off) : 0.f;
;                         w[4 * g + 2] = vd_[2] ? __builtin_amdgcn_exp2f(ls[2] + (off + s2)) : 0.f;
;                         w[4 * g + 1] = vd_[1] ? __builtin_amdgcn_exp2f(ls[1] + (off + s1)) : 0.f;
;                         w[4 * g + 0] = vd_[0] ? __builtin_amdgcn_exp2f(ls[0] + (off + s0x)) : 0.f;
;                         carry += T + Tp;
;                     }
	v_cndmask_b32_e64 v83, 0, v171, s[4:5]
	v_add_f32_e32 v83, v83, v81
	v_sub_f32_e32 v65, v65, v66
	v_sub_f32_e32 v66, v67, v76
	v_add_f32_e32 v67, v168, v83
	v_add_f32_e32 v79, v79, v83
	v_add_f32_e32 v66, v66, v67
	v_mul_f32_e32 v67, 0x3e0293ee, v72
	v_exp_f32_e32 v79, v79
	v_med3_f32 v67, v67, s79, v196
	v_exp_f32_e32 v72, v67
	v_mul_f32_e32 v74, 0x3e0293ee, v74
	v_cndmask_b32_e64 v76, 0, v79, s[22:23]
	v_exp_f32_e32 v79, v66
	v_add_f32_e32 v66, v167, v83
	v_mul_f32_e32 v75, 0x3e0293ee, v75
	v_add_f32_e32 v160, v169, v83
	v_add_f32_e32 v65, v65, v66
	v_add_f32_e32 v66, 1.0, v72
	v_mul_f32_e32 v72, 0x3e0293ee, v73
	v_med3_f32 v74, v74, s79, v196
	v_med3_f32 v75, v75, s79, v196
	v_add_f32_e32 v78, v78, v160
	v_med3_f32 v72, v72, s79, v196
	v_exp_f32_e32 v160, v74
	v_exp_f32_e32 v163, v75
	v_exp_f32_e32 v73, v72
	v_exp_f32_e32 v78, v78
	v_add_f32_e32 v160, 1.0, v160
	v_add_f32_e32 v163, 1.0, v163
	v_add_f32_e32 v73, 1.0, v73
	v_log_f32_e32 v160, v160
	v_log_f32_e32 v163, v163
	v_log_f32_e32 v73, v73
	v_log_f32_e32 v66, v66
	v_cmp_lt_i32_e64 s[22:23], 9, v149
	v_cndmask_b32_e64 v168, 0, -v160, s[24:25]
	v_cndmask_b32_e64 v169, 0, -v163, s[26:27]
	v_cndmask_b32_e64 v78, 0, v78, s[20:21]
	v_cmp_lt_i32_e64 s[20:21], 8, v149
	v_cndmask_b32_e64 v167, 0, -v73, s[22:23]
	v_add_f32_e32 v168, v169, v168
	v_exp_f32_e32 v83, v65
	v_cndmask_b32_e64 v65, 0, -v66, s[20:21]
	v_add_f32_e32 v167, v167, v168
	v_add_f32_e32 v65, v65, v167
	v_mov_b32_e32 v170, v65
	s_nop 1
	v_permlane32_swap_b32_e32 v65, v170
	v_add_f32_e32 v64, v64, v171
	v_add_f32_e32 v64, v64, v81
	v_sub_f32_e32 v74, v74, v160
	v_sub_f32_e32 v75, v75, v163
	s_waitcnt lgkmcnt(0)
	v_cndmask_b32_e64 v81, 0, v170, s[4:5]
	v_add_f32_e32 v81, v81, v64
	v_add_f32_e32 v160, v169, v81
	v_add_f32_e32 v74, v74, v160
	v_exp_f32_e32 v74, v74
	v_sub_f32_e32 v66, v67, v66
	v_sub_f32_e32 v67, v72, v73
	v_add_f32_e32 v75, v75, v81
	v_cndmask_b32_e64 v73, 0, v74, s[24:25]
	v_add_f32_e32 v74, v168, v81
	v_add_f32_e32 v67, v67, v74
	v_mul_f32_e32 v68, 0x3e0293ee, v68
	v_exp_f32_e32 v75, v75
	v_exp_f32_e32 v67, v67
	v_med3_f32 v68, v68, s79, v196
	v_exp_f32_e32 v74, v68
	v_mul_f32_e32 v70, 0x3e0293ee, v70
	v_mul_f32_e32 v71, 0x3e0293ee, v71
	v_mul_f32_e32 v69, 0x3e0293ee, v69
	v_med3_f32 v70, v70, s79, v196
	v_med3_f32 v71, v71, s79, v196
	v_cndmask_b32_e64 v72, 0, v75, s[26:27]
	v_cndmask_b32_e64 v75, 0, v67, s[22:23]
	v_add_f32_e32 v67, v167, v81
	v_med3_f32 v69, v69, s79, v196
	v_exp_f32_e32 v160, v70
	v_exp_f32_e32 v163, v71
	v_add_f32_e32 v66, v66, v67
	v_add_f32_e32 v67, 1.0, v74
	v_exp_f32_e32 v74, v69
	v_add_f32_e32 v160, 1.0, v160
	v_add_f32_e32 v163, 1.0, v163
	v_log_f32_e32 v160, v160
	v_add_f32_e32 v74, 1.0, v74
	v_log_f32_e32 v163, v163
	v_log_f32_e32 v74, v74
	v_log_f32_e32 v67, v67
	v_cmp_lt_i32_e64 s[26:27], 2, v149
	v_cmp_lt_i32_e64 s[24:25], 1, v149
	v_cndmask_b32_e64 v169, 0, -v163, s[28:29]
	v_cndmask_b32_e64 v168, 0, -v160, s[26:27]
	v_cmp_lt_i32_e64 s[22:23], 0, v149
	v_cndmask_b32_e64 v167, 0, -v74, s[24:25]
	v_add_f32_e32 v168, v169, v168
	v_cndmask_b32_e64 v81, 0, -v67, s[22:23]
	v_add_f32_e32 v167, v167, v168
	v_add_f32_e32 v171, v81, v167
	v_mov_b32_e32 v150, v171
	s_nop 1
	v_permlane32_swap_b32_e32 v171, v150
	v_add_f32_e32 v65, v65, v170
	v_add_f32_e32 v170, v65, v64
	v_sub_f32_e32 v64, v71, v163
	v_exp_f32_e32 v66, v66
	s_waitcnt lgkmcnt(0)
; #define LAS __attribute__((address_space(3)))
; template <int BR>
; DI void unit(LAS unsigned char* lds, const bf16* __restrict__ Q, const bf16* __restrict__ Kx, const bf16* __restrict__ VT, const bf16* __restrict__ RG, const bf16* __restrict__ RG1, bf16* __restrict__ O, int b, int h, int qb) {
;     ...
;                         const float s2 = lf[3], s1 = s2 + lf[2], s0x = s1 + lf[1], T = s0x + lf[0];
;                         const float Tp = __shfl_xor(T, 32);
;                         const float off = carry + (hf == 0 ? Tp : 0.f);
;                         w[4 * g + 3] = vd_[3] ? __builtin_amdgcn_exp2f(ls[3] + off) : 0.f;
;                         w[4 * g + 2] = vd_[2] ? __builtin_amdgcn_exp2f(ls[2] + (off + s2)) : 0.f;
;                         w[4 * g + 1] = vd_[1] ? __builtin_amdgcn_exp2f(ls[1] + (off + s1)) : 0.f;
;                         w[4 * g + 0] = vd_[0] ? __builtin_amdgcn_exp2f(ls[0] + (off + s0x)) : 0.f;
;                         carry += T + Tp;
;                     }
;                 } else {
;                     const float basef = (float)tq * lg2;
; #pragma unroll
;                     for (int r = 0; r < 16; ++r) { const int c = 32 * kt + 8 * (r >> 2) + (r & 3);
;                         const float dec = __builtin_amdgcn_exp2f(basef - (float)c * lg2);
;                         w[r] = (c <= tq) ? sT[r] * dec : 0.f; }
;                 }
;                 float w0[8], w1[8];
; #pragma unroll
;                 for (int j = 0; j < 8; ++j) { w0[j] = w[j]; w1[j] = w[8 + j]; }
;                 pf[2 * kt] = __builtin_bit_cast(bf16x8, pack8(w0)); pf[2 * kt + 1] = __builtin_bit_cast(bf16x8, pack8(w1));
;             }
;             const LAS unsigned char* vb_ = lds + 2 * KBUF + buf * VBUF + r32 * VS_ + 8 * hf;
; #pragma unroll
;             for (int dt = 0; dt < 4; ++dt)
; #pragma unroll
;                 for (int sp = 0; sp < 4; ++sp) {
;                     const u32x2 lo = *(const LAS u32x2*)(vb_ + dt * 32 * VS_ + 32 * sp), hi = *(const LAS u32x2*)(vb_ + dt * 32 * VS_ + 32 * sp + 16);
;                     const bf16x8 a = __builtin_bit_cast(bf16x8, (u32x4){lo.x, lo.y, hi.x, hi.y});
;                     oT[dt] = __builtin_amdgcn_mfma_f32_32x32x16_bf16(a, pf[sp], oT[dt], 0, 0, 0);
;                 }
;             if (BR == 1) wdone = __all(carry <= -150.0f) != 0;
	v_cndmask_b32_e64 v65, 0, v150, s[4:5]
	v_add_f32_e32 v65, v65, v170
	v_add_f32_e32 v64, v64, v65
	v_exp_f32_e32 v64, v64
	v_cndmask_b32_e64 v81, 0, v66, s[20:21]
	v_sub_f32_e32 v66, v68, v67
	v_sub_f32_e32 v67, v69, v74
	v_sub_f32_e32 v68, v70, v160
	v_cndmask_b32_e64 v69, 0, v64, s[28:29]
	v_add_f32_e32 v64, v169, v65
	v_add_f32_e32 v64, v68, v64
	v_exp_f32_e32 v68, v64
	v_add_f32_e32 v64, v168, v65
	v_add_f32_e32 v64, v67, v64
	v_exp_f32_e32 v70, v64
	v_add_f32_e32 v64, v167, v65
	v_add3_u32 v160, s91, v148, v143
	v_add_f32_e32 v64, v66, v64
	v_add_u32_e32 v163, 0x8800, v160
	v_exp_f32_e32 v71, v64
	ds_read2_b64 v[64:67], v163 offset1:2
	v_cndmask_b32_e64 v74, 0, v68, s[26:27]
	v_cndmask_b32_e64 v68, 0, v70, s[24:25]
	v_cndmask_b32_e64 v70, 0, v71, s[22:23]
	v_cvt_pk_bf16_f32 v68, v70, v68
	v_cvt_pk_bf16_f32 v69, v74, v69
	v_cvt_pk_bf16_f32 v70, v81, v75
	v_cvt_pk_bf16_f32 v71, v73, v72
	ds_read2_b64 v[72:75], v163 offset0:4 offset1:6
	s_waitcnt lgkmcnt(1)
	v_mfma_f32_32x32x16_bf16 v[0:15], v[64:67], v[68:71], v[0:15]
	v_cndmask_b32_e64 v64, 0, v79, s[18:19]
	v_cndmask_b32_e64 v65, 0, v83, s[16:17]
	v_cvt_pk_bf16_f32 v64, v65, v64
	v_cvt_pk_bf16_f32 v65, v78, v76
	v_cvt_pk_bf16_f32 v66, v77, v162
	v_cvt_pk_bf16_f32 v67, v161, v82
	ds_read2_b64 v[76:79], v163 offset0:8 offset1:10
	s_waitcnt lgkmcnt(1)
	v_mfma_f32_32x32x16_bf16 v[0:15], v[72:75], v[64:67], v[0:15]
	v_cndmask_b32_e64 v72, 0, v166, s[14:15]
	v_cndmask_b32_e64 v73, 0, v80, s[12:13]
	v_cvt_pk_bf16_f32 v72, v73, v72
	v_cvt_pk_bf16_f32 v73, v164, v165
	v_cvt_pk_bf16_f32 v74, v177, v173
	v_cvt_pk_bf16_f32 v75, v172, v159
	ds_read2_b64 v[80:83], v163 offset0:12 offset1:14
	s_waitcnt lgkmcnt(1)
	v_mfma_f32_32x32x16_bf16 v[0:15], v[76:79], v[72:75], v[0:15]
	v_cndmask_b32_e64 v77, 0, v156, s[10:11]
	v_cndmask_b32_e64 v76, 0, v157, s[8:9]
	v_cndmask_b32_e32 v78, 0, v158, vcc
	v_cvt_pk_bf16_f32 v76, v78, v76
	v_cvt_pk_bf16_f32 v77, v77, v155
	v_cvt_pk_bf16_f32 v78, v154, v153
	v_cvt_pk_bf16_f32 v79, v152, v151
	v_add_u32_e32 v151, 0x9800, v160
	s_waitcnt lgkmcnt(0)
	v_mfma_f32_32x32x16_bf16 v[0:15], v[80:83], v[76:79], v[0:15]
	ds_read2_b64 v[80:83], v151 offset0:32 offset1:34
	s_waitcnt lgkmcnt(0)
	v_mfma_f32_32x32x16_bf16 v[16:31], v[80:83], v[68:71], v[16:31]
	ds_read2_b64 v[80:83], v151 offset0:36 offset1:38
	s_waitcnt lgkmcnt(0)
	v_mfma_f32_32x32x16_bf16 v[16:31], v[80:83], v[64:67], v[16:31]
	ds_read2_b64 v[80:83], v151 offset0:40 offset1:42
	s_waitcnt lgkmcnt(0)
	v_mfma_f32_32x32x16_bf16 v[16:31], v[80:83], v[72:75], v[16:31]
	ds_read2_b64 v[80:83], v151 offset0:44 offset1:46
	v_add_u32_e32 v151, 0xa800, v160
	s_waitcnt lgkmcnt(0)
	v_mfma_f32_32x32x16_bf16 v[16:31], v[80:83], v[76:79], v[16:31]
	ds_read2_b64 v[80:83], v151 offset0:64 offset1:66
	s_waitcnt lgkmcnt(0)
	v_mfma_f32_32x32x16_bf16 v[32:47], v[80:83], v[68:71], v[32:47]
	ds_read2_b64 v[80:83], v151 offset0:68 offset1:70
	s_waitcnt lgkmcnt(0)
	v_mfma_f32_32x32x16_bf16 v[32:47], v[80:83], v[64:67], v[32:47]
	ds_read2_b64 v[80:83], v151 offset0:72 offset1:74
	s_waitcnt lgkmcnt(0)
	v_mfma_f32_32x32x16_bf16 v[32:47], v[80:83], v[72:75], v[32:47]
	ds_read2_b64 v[80:83], v151 offset0:76 offset1:78
	v_add_u32_e32 v151, 0xb800, v160
	s_waitcnt lgkmcnt(0)
	v_mfma_f32_32x32x16_bf16 v[32:47], v[80:83], v[76:79], v[32:47]
	ds_read2_b64 v[80:83], v151 offset0:96 offset1:98
	s_waitcnt lgkmcnt(0)
	v_mfma_f32_32x32x16_bf16 v[48:63], v[80:83], v[68:71], v[48:63]
	ds_read2_b64 v[68:71], v151 offset0:100 offset1:102
	s_waitcnt lgkmcnt(0)
	v_mfma_f32_32x32x16_bf16 v[48:63], v[68:71], v[64:67], v[48:63]
	ds_read2_b64 v[64:67], v151 offset0:104 offset1:106
	v_add_f32_e32 v68, v171, v150
	v_add_f32_e32 v80, v68, v170
	v_cmp_ge_f32_e32 vcc, s80, v80
	s_cmp_eq_u64 vcc, exec
	s_cselect_b64 s[8:9], -1, 0
	s_waitcnt lgkmcnt(0)
	v_mfma_f32_32x32x16_bf16 v[48:63], v[64:67], v[72:75], v[48:63]
	ds_read2_b64 v[64:67], v151 offset0:108 offset1:110
	s_waitcnt lgkmcnt(0)
	v_mfma_f32_32x32x16_bf16 v[48:63], v[64:67], v[76:79], v[48:63]
